# S4 + sc0 sc1 (write-through) on K1/K2 global stores to shrink the end-of-kernel L2 writeback
# baseline (speedup 1.0000x reference)
.LBB0_2:
	s_or_b64 exec, exec, s[4:5]
	s_waitcnt lgkmcnt(0)
	s_barrier
	s_and_saveexec_b64 s[2:3], vcc
	s_cbranch_execz .LBB0_7
	v_lshl_or_b32 v38, v85, 13, v66
	ds_read2st64_b32 v[34:35], v38 offset1:1
	ds_read2st64_b32 v[36:37], v38 offset0:2 offset1:3
	ds_read2st64_b32 v[54:55], v38 offset0:6 offset1:7
	ds_read2st64_b32 v[56:57], v38 offset0:4 offset1:5
	ds_read2st64_b32 v[58:59], v38 offset0:8 offset1:9
	ds_read2st64_b32 v[60:61], v38 offset0:10 offset1:11
	ds_read2st64_b32 v[62:63], v38 offset0:12 offset1:13
	ds_read2st64_b32 v[64:65], v38 offset0:14 offset1:15
	s_load_dwordx2 s[2:3], s[0:1], 0x18
	ds_read2st64_b32 v[68:69], v38 offset0:16 offset1:17
	ds_read2st64_b32 v[52:53], v38 offset0:18 offset1:19
	ds_read2st64_b32 v[48:49], v38 offset0:20 offset1:21
	ds_read2st64_b32 v[50:51], v38 offset0:22 offset1:23
	ds_read2st64_b32 v[46:47], v38 offset0:24 offset1:25
	ds_read2st64_b32 v[44:45], v38 offset0:26 offset1:27
	ds_read2st64_b32 v[40:41], v38 offset0:28 offset1:29
	ds_read2st64_b32 v[42:43], v38 offset0:30 offset1:31
	s_waitcnt lgkmcnt(0)
	v_add_f32_e32 v66, v18, v34
	v_add_f32_e32 v58, v26, v58
	v_add_f32_e32 v26, v33, v65
	v_add_f32_e32 v65, v2, v68
	v_cvt_f16_f32_e32 v2, v66
	v_lshlrev_b32_e32 v38, 4, v84
	v_mov_b32_e32 v39, 0
	v_mov_b32_e32 v34, v35
	v_mov_b32_e32 v35, v36
	v_mov_b32_e32 v18, v19
	v_mov_b32_e32 v19, v20
	v_lshl_add_u64 v[72:73], s[2:3], 0, v[38:39]
	v_pk_add_f32 v[38:39], v[18:19], v[34:35]
	v_mov_b32_e32 v34, v37
	v_mov_b32_e32 v35, v56
	v_mov_b32_e32 v20, v21
	v_mov_b32_e32 v21, v22
	v_add_f32_e32 v46, v10, v46
	v_add_f32_e32 v10, v17, v43
	v_cvt_pk_f16_f32 v17, v38, v39
	v_pk_add_f32 v[34:35], v[20:21], v[34:35]
	v_add_f32_e32 v74, v25, v55
	v_pack_b32_f16 v18, v2, v17
	v_cvt_pk_f16_f32 v2, v34, v35
	v_add_f32_e32 v51, v9, v51
	v_ashrrev_i32_e32 v9, 4, v1
	s_mul_i32 s4, s8, 0xc0
	v_alignbit_b32 v19, v2, v17, 16
	v_cvt_f16_f32_e32 v17, v74
	v_add_u32_e32 v70, s4, v9
	v_mov_b32_e32 v20, v57
	v_mov_b32_e32 v21, v54
	v_mov_b32_e32 v22, v23
	v_mov_b32_e32 v23, v24
	v_pk_add_f32 v[36:37], v[22:23], v[20:21]
	v_ashrrev_i32_e32 v71, 31, v70
	v_cvt_pk_f16_f32 v21, v36, v37
	v_lshlrev_b64 v[22:23], 11, v[70:71]
	v_alignbit_b32 v20, v21, v2, 16
	v_alignbit_b32 v21, v17, v21, 16
	v_lshl_add_u64 v[54:55], v[72:73], 0, v[22:23]
	v_cvt_f16_f32_e32 v2, v58
	global_store_dwordx4 v[54:55], v[18:21], off sc0 sc1
	v_mov_b32_e32 v22, v31
	v_mov_b32_e32 v23, v32
	v_mov_b32_e32 v18, v59
	v_mov_b32_e32 v19, v60
	v_mov_b32_e32 v20, v27
	v_mov_b32_e32 v21, v28
	v_pk_add_f32 v[24:25], v[20:21], v[18:19]
	v_mov_b32_e32 v18, v61
	v_mov_b32_e32 v19, v62
	v_mov_b32_e32 v20, v29
	v_mov_b32_e32 v21, v30
	v_cvt_pk_f16_f32 v17, v24, v25
	v_pk_add_f32 v[20:21], v[20:21], v[18:19]
	v_pack_b32_f16 v28, v2, v17
	v_cvt_pk_f16_f32 v2, v20, v21
	v_alignbit_b32 v29, v2, v17, 16
	v_cvt_f16_f32_e32 v17, v26
	v_mov_b32_e32 v18, v63
	v_mov_b32_e32 v19, v64
	v_pk_add_f32 v[22:23], v[22:23], v[18:19]
	s_nop 0
	v_cvt_pk_f16_f32 v18, v22, v23
	v_alignbit_b32 v30, v18, v2, 16
	v_alignbit_b32 v31, v17, v18, 16
	v_or_b32_e32 v18, 1, v70
	v_ashrrev_i32_e32 v19, 31, v18
	v_lshlrev_b64 v[18:19], 11, v[18:19]
	v_lshl_add_u64 v[18:19], v[72:73], 0, v[18:19]
	v_cvt_f16_f32_e32 v17, v65
	global_store_dwordx4 v[18:19], v[28:31], off sc0 sc1
	v_mov_b32_e32 v2, v3
	v_mov_b32_e32 v3, v4
	v_mov_b32_e32 v28, v69
	v_mov_b32_e32 v29, v52
	v_mov_b32_e32 v30, v53
	v_mov_b32_e32 v31, v48
	v_mov_b32_e32 v4, v5
	v_mov_b32_e32 v5, v6
	v_mov_b32_e32 v6, v7
	v_mov_b32_e32 v7, v8
	v_cvt_f16_f32_e32 v8, v51
	v_pk_add_f32 v[28:29], v[2:3], v[28:29]
	v_pk_add_f32 v[30:31], v[4:5], v[30:31]
	v_mov_b32_e32 v4, v49
	v_mov_b32_e32 v5, v50
	v_cvt_pk_f16_f32 v3, v28, v29
	v_pk_add_f32 v[6:7], v[6:7], v[4:5]
	v_pack_b32_f16 v2, v17, v3
	v_cvt_pk_f16_f32 v17, v30, v31
	v_cvt_pk_f16_f32 v5, v6, v7
	v_alignbit_b32 v3, v17, v3, 16
	v_alignbit_b32 v4, v5, v17, 16
	v_alignbit_b32 v5, v8, v5, 16
	global_store_dwordx4 v[54:55], v[2:5], off offset:1024 sc0 sc1
	v_cvt_f16_f32_e32 v8, v46
	v_mul_f32_e32 v17, v82, v28
	v_mov_b32_e32 v2, v47
	v_mov_b32_e32 v3, v44
	v_mov_b32_e32 v4, v11
	v_mov_b32_e32 v5, v12
	v_pk_add_f32 v[32:33], v[4:5], v[2:3]
	v_mov_b32_e32 v5, v40
	v_mov_b32_e32 v12, v13
	v_mov_b32_e32 v13, v14
	v_mov_b32_e32 v40, v41
	v_mov_b32_e32 v41, v42
	v_mov_b32_e32 v14, v15
	v_mov_b32_e32 v15, v16
	v_mbcnt_lo_u32_b32 v42, -1, 0
	v_cvt_pk_f16_f32 v3, v32, v33
	v_mov_b32_e32 v4, v45
	v_pk_add_f32 v[14:15], v[14:15], v[40:41]
	v_mul_f32_e32 v41, v83, v32
	v_mul_f32_e32 v32, v82, v32
	v_mbcnt_hi_u32_b32 v42, -1, v42
	v_pk_add_f32 v[12:13], v[12:13], v[4:5]
	v_fmac_f32_e32 v41, v80, v24
	v_fmac_f32_e32 v32, v81, v24
	v_mul_f32_e32 v24, v83, v33
	v_mul_f32_e32 v33, v82, v33
	v_and_b32_e32 v43, 64, v42
	v_cvt_pk_f16_f32 v4, v12, v13
	v_fmac_f32_e32 v24, v80, v25
	v_fmac_f32_e32 v33, v81, v25
	v_mul_f32_e32 v25, v83, v12
	v_mul_f32_e32 v12, v82, v12
	v_add_u32_e32 v43, 64, v43
	v_xor_b32_e32 v45, 16, v42
	v_pack_b32_f16 v2, v8, v3
	v_mul_f32_e32 v8, v83, v65
	v_mul_f32_e32 v11, v82, v65
	v_mul_f32_e32 v16, v83, v28
	v_fmac_f32_e32 v25, v80, v20
	v_fmac_f32_e32 v12, v81, v20
	v_mul_f32_e32 v20, v83, v13
	v_mul_f32_e32 v13, v82, v13
	v_and_b32_e32 v44, 16, v0
	v_cmp_lt_i32_e32 vcc, v45, v43
	v_cvt_pk_f16_f32 v5, v14, v15
	v_fmac_f32_e32 v8, v80, v66
	v_fmac_f32_e32 v11, v81, v66
	v_fmac_f32_e32 v16, v80, v38
	v_fmac_f32_e32 v17, v81, v38
	v_mul_f32_e32 v27, v83, v29
	v_mul_f32_e32 v28, v82, v29
	v_fmac_f32_e32 v20, v80, v21
	v_fmac_f32_e32 v13, v81, v21
	v_mul_f32_e32 v21, v83, v14
	v_mul_f32_e32 v14, v82, v14
	v_cndmask_b32_e32 v45, v42, v45, vcc
	v_cmp_eq_u32_e32 vcc, 0, v44
	v_fmac_f32_e32 v27, v80, v39
	v_fmac_f32_e32 v28, v81, v39
	v_mul_f32_e32 v29, v83, v30
	v_mul_f32_e32 v30, v82, v30
	v_fmac_f32_e32 v21, v80, v22
	v_fmac_f32_e32 v14, v81, v22
	v_mul_f32_e32 v22, v83, v15
	v_mul_f32_e32 v15, v82, v15
	v_lshlrev_b32_e32 v45, 2, v45
	v_cndmask_b32_e32 v44, v8, v11, vcc
	v_cndmask_b32_e32 v8, v11, v8, vcc
	v_cndmask_b32_e32 v11, v16, v17, vcc
	v_fmac_f32_e32 v29, v80, v34
	v_fmac_f32_e32 v30, v81, v34
	v_mul_f32_e32 v39, v83, v46
	v_mul_f32_e32 v40, v82, v46
	v_fmac_f32_e32 v22, v80, v23
	v_fmac_f32_e32 v15, v81, v23
	v_mul_f32_e32 v23, v83, v10
	v_mul_f32_e32 v46, v82, v10
	v_cndmask_b32_e32 v16, v17, v16, vcc
	ds_bpermute_b32 v11, v45, v11
	v_cndmask_b32_e32 v17, v27, v28, vcc
	v_fmac_f32_e32 v23, v80, v26
	v_fmac_f32_e32 v46, v81, v26
	ds_bpermute_b32 v17, v45, v17
	v_cndmask_b32_e32 v26, v29, v30, vcc
	ds_bpermute_b32 v26, v45, v26
	v_mul_f32_e32 v34, v83, v31
	v_mul_f32_e32 v31, v82, v31
	v_fmac_f32_e32 v34, v80, v35
	v_fmac_f32_e32 v31, v81, v35
	v_mul_f32_e32 v35, v83, v6
	v_mul_f32_e32 v6, v82, v6
	s_waitcnt lgkmcnt(2)
	v_add_f32_e32 v11, v16, v11
	v_cndmask_b32_e32 v16, v28, v27, vcc
	v_fmac_f32_e32 v35, v80, v36
	v_fmac_f32_e32 v6, v81, v36
	v_mul_f32_e32 v36, v83, v7
	v_mul_f32_e32 v7, v82, v7
	s_waitcnt lgkmcnt(1)
	v_add_f32_e32 v16, v16, v17
	v_cndmask_b32_e32 v17, v30, v29, vcc
	v_fmac_f32_e32 v36, v80, v37
	v_fmac_f32_e32 v7, v81, v37
	s_waitcnt lgkmcnt(0)
	v_add_f32_e32 v17, v17, v26
	v_cndmask_b32_e32 v26, v34, v31, vcc
	ds_bpermute_b32 v26, v45, v26
	v_cndmask_b32_e32 v29, v36, v7, vcc
	ds_bpermute_b32 v29, v45, v29
	v_mul_f32_e32 v37, v83, v51
	v_mul_f32_e32 v38, v82, v51
	v_fmac_f32_e32 v37, v80, v74
	v_fmac_f32_e32 v38, v81, v74
	v_cndmask_b32_e32 v27, v31, v34, vcc
	v_cndmask_b32_e32 v28, v35, v6, vcc
	v_fmac_f32_e32 v39, v80, v58
	v_fmac_f32_e32 v40, v81, v58
	ds_bpermute_b32 v28, v45, v28
	s_waitcnt lgkmcnt(2)
	v_add_f32_e32 v26, v27, v26
	v_cndmask_b32_e32 v7, v7, v36, vcc
	v_cndmask_b32_e32 v27, v37, v38, vcc
	s_waitcnt lgkmcnt(1)
	v_add_f32_e32 v7, v7, v29
	ds_bpermute_b32 v27, v45, v27
	v_cndmask_b32_e32 v29, v39, v40, vcc
	ds_bpermute_b32 v29, v45, v29
	v_cndmask_b32_e32 v6, v6, v35, vcc
	s_waitcnt lgkmcnt(2)
	v_add_f32_e32 v6, v6, v28
	v_cndmask_b32_e32 v28, v38, v37, vcc
	s_waitcnt lgkmcnt(1)
	v_add_f32_e32 v27, v28, v27
	v_cndmask_b32_e32 v28, v40, v39, vcc
	v_cndmask_b32_e32 v30, v41, v32, vcc
	s_waitcnt lgkmcnt(0)
	v_add_f32_e32 v28, v28, v29
	v_cndmask_b32_e32 v29, v32, v41, vcc
	v_cndmask_b32_e32 v32, v20, v13, vcc
	v_cndmask_b32_e32 v13, v13, v20, vcc
	v_cndmask_b32_e32 v20, v21, v14, vcc
	v_cndmask_b32_e32 v14, v14, v21, vcc
	v_cndmask_b32_e32 v21, v22, v15, vcc
	ds_bpermute_b32 v30, v45, v30
	ds_bpermute_b32 v20, v45, v20
	ds_bpermute_b32 v21, v45, v21
	ds_bpermute_b32 v44, v45, v44
	v_cndmask_b32_e32 v15, v15, v22, vcc
	v_xor_b32_e32 v22, 8, v42
	s_waitcnt lgkmcnt(3)
	v_add_f32_e32 v29, v29, v30
	v_cndmask_b32_e32 v30, v24, v33, vcc
	v_cndmask_b32_e32 v24, v33, v24, vcc
	v_cndmask_b32_e32 v31, v25, v12, vcc
	v_cndmask_b32_e32 v12, v12, v25, vcc
	v_cndmask_b32_e32 v25, v23, v46, vcc
	s_waitcnt lgkmcnt(2)
	v_add_f32_e32 v14, v14, v20
	s_waitcnt lgkmcnt(1)
	v_add_f32_e32 v15, v15, v21
	v_cndmask_b32_e32 v20, v46, v23, vcc
	v_and_b32_e32 v21, 8, v0
	v_cmp_lt_i32_e32 vcc, v22, v43
	s_waitcnt lgkmcnt(0)
	v_add_f32_e32 v8, v8, v44
	ds_bpermute_b32 v31, v45, v31
	v_cndmask_b32_e32 v22, v42, v22, vcc
	v_cmp_eq_u32_e32 vcc, 0, v21
	v_lshlrev_b32_e32 v22, 2, v22
	ds_bpermute_b32 v32, v45, v32
	v_cndmask_b32_e32 v21, v8, v28, vcc
	ds_bpermute_b32 v21, v22, v21
	v_cndmask_b32_e32 v23, v11, v29, vcc
	ds_bpermute_b32 v30, v45, v30
	ds_bpermute_b32 v23, v22, v23
	s_waitcnt lgkmcnt(4)
	v_add_f32_e32 v12, v12, v31
	ds_bpermute_b32 v25, v45, v25
	v_cndmask_b32_e32 v8, v28, v8, vcc
	s_waitcnt lgkmcnt(4)
	v_add_f32_e32 v13, v13, v32
	s_waitcnt lgkmcnt(3)
	v_add_f32_e32 v8, v8, v21
	v_cndmask_b32_e32 v21, v17, v12, vcc
	v_cndmask_b32_e32 v12, v12, v17, vcc
	ds_bpermute_b32 v17, v22, v21
	v_cndmask_b32_e32 v21, v26, v13, vcc
	v_cndmask_b32_e32 v11, v29, v11, vcc
	ds_bpermute_b32 v21, v22, v21
	s_waitcnt lgkmcnt(4)
	v_add_f32_e32 v24, v24, v30
	s_waitcnt lgkmcnt(3)
	v_add_f32_e32 v11, v11, v23
	v_cndmask_b32_e32 v23, v6, v14, vcc
	s_waitcnt lgkmcnt(2)
	v_add_f32_e32 v20, v20, v25
	v_cndmask_b32_e32 v25, v16, v24, vcc
	ds_bpermute_b32 v23, v22, v23
	v_cndmask_b32_e32 v6, v14, v6, vcc
	v_cndmask_b32_e32 v14, v7, v15, vcc
	ds_bpermute_b32 v25, v22, v25
	ds_bpermute_b32 v14, v22, v14
	v_cndmask_b32_e32 v13, v13, v26, vcc
	v_cndmask_b32_e32 v7, v15, v7, vcc
	v_cndmask_b32_e32 v15, v27, v20, vcc
	s_waitcnt lgkmcnt(3)
	v_add_f32_e32 v13, v13, v21
	ds_bpermute_b32 v15, v22, v15
	v_xor_b32_e32 v21, 4, v42
	v_add_f32_e32 v12, v12, v17
	v_and_b32_e32 v17, 4, v0
	v_cmp_lt_i32_e64 s[2:3], v21, v43
	v_cndmask_b32_e32 v16, v24, v16, vcc
	s_waitcnt lgkmcnt(3)
	v_add_f32_e32 v6, v6, v23
	v_cndmask_b32_e64 v21, v42, v21, s[2:3]
	v_cmp_eq_u32_e64 s[2:3], 0, v17
	s_waitcnt lgkmcnt(2)
	v_add_f32_e32 v16, v16, v25
	v_lshlrev_b32_e32 v21, 2, v21
	v_cndmask_b32_e64 v17, v8, v13, s[2:3]
	s_waitcnt lgkmcnt(1)
	v_add_f32_e32 v7, v7, v14
	v_cndmask_b32_e64 v8, v13, v8, s[2:3]
	v_cndmask_b32_e64 v13, v11, v6, s[2:3]
	v_cndmask_b32_e32 v14, v20, v27, vcc
	v_cndmask_b32_e64 v6, v6, v11, s[2:3]
	ds_bpermute_b32 v11, v21, v13
	v_cndmask_b32_e64 v13, v16, v7, s[2:3]
	s_waitcnt lgkmcnt(1)
	v_add_f32_e32 v14, v14, v15
	ds_bpermute_b32 v13, v21, v13
	v_cndmask_b32_e64 v15, v12, v14, s[2:3]
	ds_bpermute_b32 v17, v21, v17
	ds_bpermute_b32 v15, v21, v15
	v_cndmask_b32_e64 v7, v7, v16, s[2:3]
	s_waitcnt lgkmcnt(2)
	v_add_f32_e32 v7, v7, v13
	v_xor_b32_e32 v13, 2, v42
	v_add_f32_e32 v6, v6, v11
	v_cndmask_b32_e64 v11, v14, v12, s[2:3]
	v_and_b32_e32 v12, 2, v0
	v_cmp_lt_i32_e32 vcc, v13, v43
	s_waitcnt lgkmcnt(1)
	v_add_f32_e32 v8, v8, v17
	s_waitcnt lgkmcnt(0)
	v_add_f32_e32 v11, v11, v15
	v_cndmask_b32_e32 v13, v42, v13, vcc
	v_cmp_eq_u32_e32 vcc, 0, v12
	v_lshlrev_b32_e32 v13, 2, v13
	v_cvt_f16_f32_e32 v10, v10
	v_cndmask_b32_e32 v12, v8, v7, vcc
	v_cndmask_b32_e32 v14, v6, v11, vcc
	ds_bpermute_b32 v12, v13, v12
	ds_bpermute_b32 v13, v13, v14
	v_cndmask_b32_e32 v6, v11, v6, vcc
	v_xor_b32_e32 v11, 1, v42
	v_cndmask_b32_e32 v7, v7, v8, vcc
	v_and_b32_e32 v8, 1, v0
	v_cmp_lt_i32_e32 vcc, v11, v43
	s_waitcnt lgkmcnt(1)
	v_add_f32_e32 v7, v7, v12
	s_waitcnt lgkmcnt(0)
	v_add_f32_e32 v6, v6, v13
	v_cndmask_b32_e32 v11, v42, v11, vcc
	v_cmp_eq_u32_e32 vcc, 0, v8
	v_lshlrev_b32_e32 v11, 2, v11
	v_alignbit_b32 v3, v4, v3, 16
	v_cndmask_b32_e32 v8, v7, v6, vcc
	ds_bpermute_b32 v8, v11, v8
	v_alignbit_b32 v4, v5, v4, 16
	v_alignbit_b32 v5, v10, v5, 16
	global_store_dwordx4 v[18:19], v[2:5], off offset:1024 sc0 sc1
	s_nop 1
	v_cndmask_b32_e32 v2, v6, v7, vcc
	s_waitcnt lgkmcnt(0)
	v_add_f32_e32 v2, v2, v8
	v_cmp_lt_u32_e32 vcc, 15, v79
	s_and_saveexec_b64 s[2:3], vcc
	s_xor_b64 s[2:3], exec, s[2:3]
	s_cbranch_execz .LBB0_5
	v_mul_f32_e32 v1, 0x3fb8aa3b, v2
	v_mul_f32_e32 v2, 0x3e4ccccd, v2
	s_lshr_b32 s6, s8, 2
	v_add_u32_e32 v0, -16, v79
	v_exp_f32_e32 v1, v1
	v_mul_f32_e32 v2, 0x3fb8aa3b, v2
	v_lshrrev_b32_e32 v0, 3, v0
	s_mulk_i32 s6, 0xc0
	v_exp_f32_e32 v2, v2
	s_load_dwordx2 s[4:5], s[0:1], 0x20
	v_add_u32_e32 v0, s6, v0
	s_lshl_b32 s6, s8, 1
	v_add_lshl_u32 v0, v0, v9, 3
	s_and_b32 s6, s6, 6
	v_or3_b32 v0, v0, s6, v67
	v_cvt_f16_f32_e32 v3, v1
	v_lshl_or_b32 v0, v0, 4, v78
	v_cvt_f16_f32_e32 v2, v2
	v_ashrrev_i32_e32 v1, 31, v0
	s_waitcnt lgkmcnt(0)
	v_lshl_add_u64 v[0:1], v[0:1], 1, s[4:5]
	global_store_short v[0:1], v3, off sc0 sc1
	global_store_short v[0:1], v2, off offset:16 sc0 sc1
.LBB0_5:
	s_andn2_saveexec_b64 s[2:3], s[2:3]
	s_cbranch_execz .LBB0_7
	v_mul_f32_e32 v2, 0xbf4ccccd, v2
	v_mul_f32_e32 v2, 0x3fb8aa3b, v2
	v_exp_f32_e32 v2, v2
	v_lshlrev_b32_e32 v3, 1, v0
	s_load_dwordx2 s[0:1], s[0:1], 0x28
	v_and_b32_e32 v3, 24, v3
	v_and_or_b32 v0, v0, 3, v3
	v_lshlrev_b32_e32 v3, 2, v67
	s_mul_i32 s2, s8, 0xc00
	v_cvt_f16_f32_e32 v2, v2
	v_or3_b32 v0, v0, v3, s2
	v_add_u32_e32 v0, v0, v1
	v_ashrrev_i32_e32 v1, 31, v0
	s_waitcnt lgkmcnt(0)
	v_lshl_add_u64 v[0:1], v[0:1], 1, s[0:1]
	global_store_short v[0:1], v2, off sc0 sc1

.LBB1_16:
	s_lshl_b64 s[16:17], s[16:17], 10
	s_add_u32 s16, s14, s16
	s_addc_u32 s17, s15, s17
	v_lshlrev_b32_e32 v0, 2, v0
	global_store_dword v0, v67, s[16:17] sc0 sc1

.LBB1_30:
	s_lshl_b64 s[16:17], s[16:17], 10
	s_add_u32 s16, s14, s16
	s_addc_u32 s17, s15, s17
	v_lshlrev_b32_e32 v0, 2, v0
	global_store_dword v0, v75, s[16:17] sc0 sc1

.LBB1_45:
	ds_read2st64_b32 v[2:3], v127 offset0:112 offset1:113
	ds_read2st64_b32 v[4:5], v127 offset0:114 offset1:115
	ds_read2st64_b32 v[6:7], v127 offset0:116 offset1:117
	ds_read2st64_b32 v[8:9], v127 offset0:118 offset1:119
	v_lshlrev_b32_e32 v1, 1, v118
	v_lshlrev_b32_e32 v122, 1, v116
	s_waitcnt lgkmcnt(3)
	v_add_f32_e32 v2, v50, v2
	v_cvt_f16_f32_e32 v2, v2
	v_add_f32_e32 v3, v51, v3
	v_cvt_f16_f32_e32 v12, v3
	global_store_short v1, v2, s[18:19] sc0 sc1
	s_waitcnt lgkmcnt(2)
	v_add_f32_e32 v1, v52, v4
	v_lshl_add_u64 v[2:3], s[18:19], 0, v[122:123]
	v_cvt_f16_f32_e32 v1, v1
	v_add_f32_e32 v4, v53, v5
	v_add_co_u32_e32 v10, vcc, 0x4000, v2
	v_cvt_f16_f32_e32 v4, v4
	s_nop 0
	v_addc_co_u32_e32 v11, vcc, 0, v3, vcc
	global_store_short v[10:11], v12, off offset:512 sc0 sc1
	global_store_short v[10:11], v1, off offset:1024 sc0 sc1
	global_store_short v[10:11], v4, off offset:1536 sc0 sc1
	s_waitcnt lgkmcnt(1)
	v_add_f32_e32 v1, v54, v6
	v_cvt_f16_f32_e32 v1, v1
	v_add_co_u32_e32 v4, vcc, s37, v2
	s_waitcnt lgkmcnt(0)
	v_add_f32_e32 v6, v56, v8
	v_addc_co_u32_e32 v5, vcc, 0, v3, vcc
	v_add_co_u32_e32 v12, vcc, s38, v2
	v_cvt_f16_f32_e32 v6, v6
	s_nop 0
	v_addc_co_u32_e32 v13, vcc, 0, v3, vcc
	global_store_short v[12:13], v1, off offset:-4096 sc0 sc1
	v_add_f32_e32 v1, v55, v7
	v_cvt_f16_f32_e32 v1, v1
	v_add_f32_e32 v7, v57, v9
	v_cvt_f16_f32_e32 v8, v7
	global_store_short v[4:5], v1, off offset:512 sc0 sc1
	global_store_short v[4:5], v6, off offset:1024 sc0 sc1
	ds_read2st64_b32 v[6:7], v127 offset0:120 offset1:121
	global_store_short v[4:5], v8, off offset:1536 sc0 sc1
	ds_read2st64_b32 v[8:9], v127 offset0:122 offset1:123
	ds_read2st64_b32 v[14:15], v127 offset0:124 offset1:125
	ds_read2st64_b32 v[16:17], v127 offset0:126 offset1:127
	v_add_co_u32_e32 v2, vcc, s39, v2
	s_waitcnt lgkmcnt(3)
	v_add_f32_e32 v1, v58, v6
	v_cvt_f16_f32_e32 v1, v1
	v_add_f32_e32 v6, v59, v7
	v_cvt_f16_f32_e32 v6, v6
	s_waitcnt lgkmcnt(2)
	v_add_f32_e32 v7, v60, v8
	v_cvt_f16_f32_e32 v7, v7
	v_add_f32_e32 v8, v61, v9
	v_cvt_f16_f32_e32 v8, v8
	global_store_short v[12:13], v1, off sc0 sc1
	global_store_short v[12:13], v6, off offset:512 sc0 sc1
	global_store_short v[12:13], v7, off offset:1024 sc0 sc1
	global_store_short v[12:13], v8, off offset:1536 sc0 sc1
	s_waitcnt lgkmcnt(1)
	v_add_f32_e32 v1, v62, v14
	v_cvt_f16_f32_e32 v1, v1
	s_waitcnt lgkmcnt(0)
	v_add_f32_e32 v6, v64, v16
	v_cvt_f16_f32_e32 v34, v6
	ds_read2st64_b32 v[6:7], v127 offset0:128 offset1:129
	v_addc_co_u32_e32 v3, vcc, 0, v3, vcc
	global_store_short v[2:3], v1, off sc0 sc1
	v_add_f32_e32 v1, v63, v15
	v_cvt_f16_f32_e32 v1, v1
	v_add_f32_e32 v8, v65, v17
	v_cvt_f16_f32_e32 v35, v8
	ds_read2st64_b32 v[8:9], v127 offset0:130 offset1:131
	ds_read2st64_b32 v[14:15], v127 offset0:132 offset1:133
	ds_read2st64_b32 v[16:17], v127 offset0:134 offset1:135
	s_waitcnt lgkmcnt(3)
	v_add_f32_e32 v6, v18, v6
	v_cvt_f16_f32_e32 v6, v6
	global_store_short v[2:3], v1, off offset:512 sc0 sc1
	global_store_short v[2:3], v34, off offset:1024 sc0 sc1
	global_store_short v[2:3], v35, off offset:1536 sc0 sc1
	global_store_short v[10:11], v6, off offset:64 sc0 sc1
	v_add_f32_e32 v1, v19, v7
	v_cvt_f16_f32_e32 v1, v1
	s_waitcnt lgkmcnt(2)
	v_add_f32_e32 v6, v20, v8
	v_cvt_f16_f32_e32 v6, v6
	v_add_f32_e32 v7, v21, v9
	v_cvt_f16_f32_e32 v7, v7
	s_waitcnt lgkmcnt(1)
	v_add_f32_e32 v8, v22, v14
	v_cvt_f16_f32_e32 v8, v8
	global_store_short v[10:11], v1, off offset:576 sc0 sc1
	global_store_short v[10:11], v6, off offset:1088 sc0 sc1
	global_store_short v[10:11], v7, off offset:1600 sc0 sc1
	global_store_short v[4:5], v8, off offset:64 sc0 sc1
	v_add_f32_e32 v1, v23, v15
	v_cvt_f16_f32_e32 v1, v1
	s_waitcnt lgkmcnt(0)
	v_add_f32_e32 v6, v24, v16
	v_cvt_f16_f32_e32 v6, v6
	v_add_f32_e32 v7, v25, v17
	v_cvt_f16_f32_e32 v8, v7
	global_store_short v[4:5], v1, off offset:576 sc0 sc1
	global_store_short v[4:5], v6, off offset:1088 sc0 sc1
	ds_read2st64_b32 v[6:7], v127 offset0:136 offset1:137
	global_store_short v[4:5], v8, off offset:1600 sc0 sc1
	ds_read2st64_b32 v[4:5], v127 offset0:138 offset1:139
	ds_read2st64_b32 v[8:9], v127 offset0:140 offset1:141
	ds_read2st64_b32 v[10:11], v127 offset0:142 offset1:143
	s_waitcnt lgkmcnt(3)
	v_add_f32_e32 v1, v26, v6
	v_cvt_f16_f32_e32 v1, v1
	v_add_f32_e32 v6, v27, v7
	v_cvt_f16_f32_e32 v6, v6
	s_waitcnt lgkmcnt(2)
	v_add_f32_e32 v4, v28, v4
	v_cvt_f16_f32_e32 v4, v4
	v_add_f32_e32 v5, v29, v5
	v_cvt_f16_f32_e32 v5, v5
	global_store_short v[12:13], v1, off offset:64 sc0 sc1
	global_store_short v[12:13], v6, off offset:576 sc0 sc1
	global_store_short v[12:13], v4, off offset:1088 sc0 sc1
	global_store_short v[12:13], v5, off offset:1600 sc0 sc1
	s_waitcnt lgkmcnt(1)
	v_add_f32_e32 v1, v30, v8
	v_cvt_f16_f32_e32 v1, v1
	v_add_f32_e32 v4, v31, v9
	v_cvt_f16_f32_e32 v4, v4
	s_waitcnt lgkmcnt(0)
	v_add_f32_e32 v5, v32, v10
	v_cvt_f16_f32_e32 v5, v5
	v_add_f32_e32 v6, v33, v11
	v_cvt_f16_f32_e32 v6, v6
	global_store_short v[2:3], v1, off offset:64 sc0 sc1
	global_store_short v[2:3], v4, off offset:576 sc0 sc1
	global_store_short v[2:3], v5, off offset:1088 sc0 sc1
	global_store_short v[2:3], v6, off offset:1600 sc0 sc1
	s_and_saveexec_b64 s[24:25], s[4:5]
	s_cbranch_execz .LBB1_47
	ds_read_b32 v1, v128 offset:128
	s_mov_b64 s[20:21], exec
	s_waitcnt lgkmcnt(0)
	v_add_f32_e32 v67, v0, v1

.LBB1_48:
	ds_read2st64_b32 v[0:1], v127 offset0:80 offset1:81
	ds_read2st64_b32 v[18:19], v127 offset0:82 offset1:83
	ds_read2st64_b32 v[20:21], v127 offset0:84 offset1:85
	ds_read2st64_b32 v[22:23], v127 offset0:86 offset1:87
	v_lshlrev_b32_e32 v122, 1, v124
	v_lshl_add_u64 v[24:25], s[18:19], 0, v[122:123]
	s_waitcnt lgkmcnt(2)
	v_add_f32_e32 v18, v36, v18
	v_add_f32_e32 v0, v34, v0
	v_cvt_f16_f32_e32 v0, v0
	v_add_f32_e32 v1, v35, v1
	v_cvt_f16_f32_e32 v1, v1
	v_cvt_f16_f32_e32 v18, v18
	v_add_f32_e32 v19, v37, v19
	v_cvt_f16_f32_e32 v19, v19
	global_store_short v122, v0, s[18:19] sc0 sc1
	global_store_short v122, v1, s[18:19] offset:512 sc0 sc1
	global_store_short v122, v18, s[18:19] offset:1024 sc0 sc1
	global_store_short v122, v19, s[18:19] offset:1536 sc0 sc1
	s_waitcnt lgkmcnt(1)
	v_add_f32_e32 v0, v38, v20
	v_cvt_f16_f32_e32 v20, v0
	v_add_co_u32_e32 v0, vcc, s40, v24
	s_nop 1
	v_addc_co_u32_e32 v1, vcc, 0, v25, vcc
	v_add_co_u32_e32 v18, vcc, s35, v24
	s_nop 1
	v_addc_co_u32_e32 v19, vcc, 0, v25, vcc
	global_store_short v[18:19], v20, off offset:-4096 sc0 sc1
	v_add_f32_e32 v20, v39, v21
	v_cvt_f16_f32_e32 v20, v20
	s_waitcnt lgkmcnt(0)
	v_add_f32_e32 v21, v40, v22
	v_cvt_f16_f32_e32 v21, v21
	v_add_f32_e32 v22, v41, v23
	v_cvt_f16_f32_e32 v22, v22
	global_store_short v[0:1], v20, off offset:512 sc0 sc1
	global_store_short v[0:1], v21, off offset:1024 sc0 sc1
	ds_read2st64_b32 v[20:21], v127 offset0:88 offset1:89
	global_store_short v[0:1], v22, off offset:1536 sc0 sc1
	ds_read2st64_b32 v[22:23], v127 offset0:90 offset1:91
	ds_read2st64_b32 v[26:27], v127 offset0:92 offset1:93
	ds_read2st64_b32 v[28:29], v127 offset0:94 offset1:95
	s_waitcnt lgkmcnt(3)
	v_add_f32_e32 v20, v42, v20
	v_cvt_f16_f32_e32 v20, v20
	v_add_f32_e32 v21, v43, v21
	v_cvt_f16_f32_e32 v21, v21
	s_waitcnt lgkmcnt(2)
	v_add_f32_e32 v22, v44, v22
	v_cvt_f16_f32_e32 v22, v22
	v_add_f32_e32 v23, v45, v23
	v_cvt_f16_f32_e32 v23, v23
	global_store_short v[18:19], v20, off sc0 sc1
	global_store_short v[18:19], v21, off offset:512 sc0 sc1
	global_store_short v[18:19], v22, off offset:1024 sc0 sc1
	global_store_short v[18:19], v23, off offset:1536 sc0 sc1
	s_waitcnt lgkmcnt(1)
	v_add_f32_e32 v20, v46, v26
	v_cvt_f16_f32_e32 v22, v20
	v_add_co_u32_e32 v20, vcc, s41, v24
	s_waitcnt lgkmcnt(0)
	v_add_f32_e32 v24, v49, v29
	v_addc_co_u32_e32 v21, vcc, 0, v25, vcc
	global_store_short v[20:21], v22, off sc0 sc1
	v_add_f32_e32 v22, v47, v27
	v_cvt_f16_f32_e32 v30, v22
	v_add_f32_e32 v22, v48, v28
	v_cvt_f16_f32_e32 v31, v22
	ds_read2st64_b32 v[22:23], v127 offset0:96 offset1:97
	v_cvt_f16_f32_e32 v32, v24
	ds_read2st64_b32 v[24:25], v127 offset0:98 offset1:99
	ds_read2st64_b32 v[26:27], v127 offset0:100 offset1:101
	ds_read2st64_b32 v[28:29], v127 offset0:102 offset1:103
	s_waitcnt lgkmcnt(3)
	v_add_f32_e32 v2, v2, v22
	v_cvt_f16_f32_e32 v2, v2
	global_store_short v[20:21], v30, off offset:512 sc0 sc1
	global_store_short v[20:21], v31, off offset:1024 sc0 sc1
	global_store_short v[20:21], v32, off offset:1536 sc0 sc1
	global_store_short v122, v2, s[18:19] offset:64 sc0 sc1
	v_add_f32_e32 v2, v3, v23
	v_cvt_f16_f32_e32 v2, v2
	s_waitcnt lgkmcnt(2)
	v_add_f32_e32 v3, v4, v24
	v_cvt_f16_f32_e32 v3, v3
	v_add_f32_e32 v4, v5, v25
	v_cvt_f16_f32_e32 v4, v4
	s_waitcnt lgkmcnt(1)
	v_add_f32_e32 v5, v6, v26
	v_cvt_f16_f32_e32 v5, v5
	global_store_short v122, v2, s[18:19] offset:576 sc0 sc1
	global_store_short v122, v3, s[18:19] offset:1088 sc0 sc1
	global_store_short v122, v4, s[18:19] offset:1600 sc0 sc1
	global_store_short v[0:1], v5, off offset:64 sc0 sc1
	v_add_f32_e32 v2, v7, v27
	v_cvt_f16_f32_e32 v2, v2
	s_waitcnt lgkmcnt(0)
	v_add_f32_e32 v3, v8, v28
	v_cvt_f16_f32_e32 v3, v3
	v_add_f32_e32 v4, v9, v29
	v_cvt_f16_f32_e32 v4, v4
	global_store_short v[0:1], v2, off offset:576 sc0 sc1
	global_store_short v[0:1], v3, off offset:1088 sc0 sc1
	ds_read2st64_b32 v[2:3], v127 offset0:104 offset1:105
	s_mov_b64 s[18:19], s[20:21]
	global_store_short v[0:1], v4, off offset:1600 sc0 sc1
	ds_read2st64_b32 v[0:1], v127 offset0:106 offset1:107
	ds_read2st64_b32 v[4:5], v127 offset0:108 offset1:109
	ds_read2st64_b32 v[6:7], v127 offset0:110 offset1:111
	s_waitcnt lgkmcnt(3)
	v_add_f32_e32 v2, v10, v2
	v_cvt_f16_f32_e32 v2, v2
	v_add_f32_e32 v3, v11, v3
	v_cvt_f16_f32_e32 v3, v3
	s_waitcnt lgkmcnt(2)
	v_add_f32_e32 v0, v12, v0
	v_cvt_f16_f32_e32 v0, v0
	v_add_f32_e32 v1, v13, v1
	v_cvt_f16_f32_e32 v1, v1
	global_store_short v[18:19], v2, off offset:64 sc0 sc1
	global_store_short v[18:19], v3, off offset:576 sc0 sc1
	global_store_short v[18:19], v0, off offset:1088 sc0 sc1
	global_store_short v[18:19], v1, off offset:1600 sc0 sc1
	s_waitcnt lgkmcnt(1)
	v_add_f32_e32 v0, v14, v4
	v_cvt_f16_f32_e32 v0, v0
	v_add_f32_e32 v1, v15, v5
	v_cvt_f16_f32_e32 v1, v1
	s_waitcnt lgkmcnt(0)
	v_add_f32_e32 v2, v16, v6
	v_cvt_f16_f32_e32 v2, v2
	v_add_f32_e32 v3, v17, v7
	v_cvt_f16_f32_e32 v3, v3
	global_store_short v[20:21], v0, off offset:64 sc0 sc1
	global_store_short v[20:21], v1, off offset:576 sc0 sc1
	global_store_short v[20:21], v2, off offset:1088 sc0 sc1
	global_store_short v[20:21], v3, off offset:1600 sc0 sc1
	s_and_saveexec_b64 s[24:25], s[4:5]
	s_cbranch_execz .LBB1_50
	ds_read_b32 v0, v128
	s_or_b64 s[18:19], s[20:21], exec
	s_waitcnt lgkmcnt(0)
	v_add_f32_e32 v67, v66, v0

.LBB1_51:
	ds_read2st64_b32 v[2:3], v127 offset0:112 offset1:113
	ds_read2st64_b32 v[4:5], v127 offset0:114 offset1:115
	ds_read2st64_b32 v[6:7], v127 offset0:116 offset1:117
	ds_read2st64_b32 v[8:9], v127 offset0:118 offset1:119
	v_lshlrev_b32_e32 v1, 1, v118
	v_lshlrev_b32_e32 v122, 1, v116
	s_waitcnt lgkmcnt(3)
	v_add_f32_e32 v2, v50, v2
	v_cvt_f16_f32_e32 v2, v2
	v_add_f32_e32 v3, v51, v3
	v_cvt_f16_f32_e32 v12, v3
	global_store_short v1, v2, s[18:19] sc0 sc1
	s_waitcnt lgkmcnt(2)
	v_add_f32_e32 v1, v52, v4
	v_lshl_add_u64 v[2:3], s[18:19], 0, v[122:123]
	v_cvt_f16_f32_e32 v1, v1
	v_add_f32_e32 v4, v53, v5
	v_add_co_u32_e32 v10, vcc, 0x4000, v2
	v_cvt_f16_f32_e32 v4, v4
	s_nop 0
	v_addc_co_u32_e32 v11, vcc, 0, v3, vcc
	global_store_short v[10:11], v12, off offset:512 sc0 sc1
	global_store_short v[10:11], v1, off offset:1024 sc0 sc1
	global_store_short v[10:11], v4, off offset:1536 sc0 sc1
	s_waitcnt lgkmcnt(1)
	v_add_f32_e32 v1, v54, v6
	v_cvt_f16_f32_e32 v1, v1
	v_add_co_u32_e32 v4, vcc, s37, v2
	s_waitcnt lgkmcnt(0)
	v_add_f32_e32 v6, v56, v8
	v_addc_co_u32_e32 v5, vcc, 0, v3, vcc
	v_add_co_u32_e32 v12, vcc, s38, v2
	v_cvt_f16_f32_e32 v6, v6
	s_nop 0
	v_addc_co_u32_e32 v13, vcc, 0, v3, vcc
	global_store_short v[12:13], v1, off offset:-4096 sc0 sc1
	v_add_f32_e32 v1, v55, v7
	v_cvt_f16_f32_e32 v1, v1
	v_add_f32_e32 v7, v57, v9
	v_cvt_f16_f32_e32 v8, v7
	global_store_short v[4:5], v1, off offset:512 sc0 sc1
	global_store_short v[4:5], v6, off offset:1024 sc0 sc1
	ds_read2st64_b32 v[6:7], v127 offset0:120 offset1:121
	global_store_short v[4:5], v8, off offset:1536 sc0 sc1
	ds_read2st64_b32 v[8:9], v127 offset0:122 offset1:123
	ds_read2st64_b32 v[14:15], v127 offset0:124 offset1:125
	ds_read2st64_b32 v[16:17], v127 offset0:126 offset1:127
	v_add_co_u32_e32 v2, vcc, s39, v2
	s_waitcnt lgkmcnt(3)
	v_add_f32_e32 v1, v58, v6
	v_cvt_f16_f32_e32 v1, v1
	v_add_f32_e32 v6, v59, v7
	v_cvt_f16_f32_e32 v6, v6
	s_waitcnt lgkmcnt(2)
	v_add_f32_e32 v7, v60, v8
	v_cvt_f16_f32_e32 v7, v7
	v_add_f32_e32 v8, v61, v9
	v_cvt_f16_f32_e32 v8, v8
	global_store_short v[12:13], v1, off sc0 sc1
	global_store_short v[12:13], v6, off offset:512 sc0 sc1
	global_store_short v[12:13], v7, off offset:1024 sc0 sc1
	global_store_short v[12:13], v8, off offset:1536 sc0 sc1
	s_waitcnt lgkmcnt(1)
	v_add_f32_e32 v1, v62, v14
	v_cvt_f16_f32_e32 v1, v1
	s_waitcnt lgkmcnt(0)
	v_add_f32_e32 v6, v64, v16
	v_cvt_f16_f32_e32 v34, v6
	ds_read2st64_b32 v[6:7], v127 offset0:128 offset1:129
	v_addc_co_u32_e32 v3, vcc, 0, v3, vcc
	global_store_short v[2:3], v1, off sc0 sc1
	v_add_f32_e32 v1, v63, v15
	v_cvt_f16_f32_e32 v1, v1
	v_add_f32_e32 v8, v65, v17
	v_cvt_f16_f32_e32 v35, v8
	ds_read2st64_b32 v[8:9], v127 offset0:130 offset1:131
	ds_read2st64_b32 v[14:15], v127 offset0:132 offset1:133
	ds_read2st64_b32 v[16:17], v127 offset0:134 offset1:135
	s_waitcnt lgkmcnt(3)
	v_add_f32_e32 v6, v18, v6
	v_cvt_f16_f32_e32 v6, v6
	global_store_short v[2:3], v1, off offset:512 sc0 sc1
	global_store_short v[2:3], v34, off offset:1024 sc0 sc1
	global_store_short v[2:3], v35, off offset:1536 sc0 sc1
	global_store_short v[10:11], v6, off offset:64 sc0 sc1
	v_add_f32_e32 v1, v19, v7
	v_cvt_f16_f32_e32 v1, v1
	s_waitcnt lgkmcnt(2)
	v_add_f32_e32 v6, v20, v8
	v_cvt_f16_f32_e32 v6, v6
	v_add_f32_e32 v7, v21, v9
	v_cvt_f16_f32_e32 v7, v7
	s_waitcnt lgkmcnt(1)
	v_add_f32_e32 v8, v22, v14
	v_cvt_f16_f32_e32 v8, v8
	global_store_short v[10:11], v1, off offset:576 sc0 sc1
	global_store_short v[10:11], v6, off offset:1088 sc0 sc1
	global_store_short v[10:11], v7, off offset:1600 sc0 sc1
	global_store_short v[4:5], v8, off offset:64 sc0 sc1
	v_add_f32_e32 v1, v23, v15
	v_cvt_f16_f32_e32 v1, v1
	s_waitcnt lgkmcnt(0)
	v_add_f32_e32 v6, v24, v16
	v_cvt_f16_f32_e32 v6, v6
	v_add_f32_e32 v7, v25, v17
	v_cvt_f16_f32_e32 v8, v7
	global_store_short v[4:5], v1, off offset:576 sc0 sc1
	global_store_short v[4:5], v6, off offset:1088 sc0 sc1
	ds_read2st64_b32 v[6:7], v127 offset0:136 offset1:137
	global_store_short v[4:5], v8, off offset:1600 sc0 sc1
	ds_read2st64_b32 v[4:5], v127 offset0:138 offset1:139
	ds_read2st64_b32 v[8:9], v127 offset0:140 offset1:141
	ds_read2st64_b32 v[10:11], v127 offset0:142 offset1:143
	s_waitcnt lgkmcnt(3)
	v_add_f32_e32 v1, v26, v6
	v_cvt_f16_f32_e32 v1, v1
	v_add_f32_e32 v6, v27, v7
	v_cvt_f16_f32_e32 v6, v6
	s_waitcnt lgkmcnt(2)
	v_add_f32_e32 v4, v28, v4
	v_cvt_f16_f32_e32 v4, v4
	v_add_f32_e32 v5, v29, v5
	v_cvt_f16_f32_e32 v5, v5
	global_store_short v[12:13], v1, off offset:64 sc0 sc1
	global_store_short v[12:13], v6, off offset:576 sc0 sc1
	global_store_short v[12:13], v4, off offset:1088 sc0 sc1
	global_store_short v[12:13], v5, off offset:1600 sc0 sc1
	s_waitcnt lgkmcnt(1)
	v_add_f32_e32 v1, v30, v8
	v_cvt_f16_f32_e32 v1, v1
	v_add_f32_e32 v4, v31, v9
	v_cvt_f16_f32_e32 v4, v4
	s_waitcnt lgkmcnt(0)
	v_add_f32_e32 v5, v32, v10
	v_cvt_f16_f32_e32 v5, v5
	v_add_f32_e32 v6, v33, v11
	v_cvt_f16_f32_e32 v6, v6
	global_store_short v[2:3], v1, off offset:64 sc0 sc1
	global_store_short v[2:3], v4, off offset:576 sc0 sc1
	global_store_short v[2:3], v5, off offset:1088 sc0 sc1
	global_store_short v[2:3], v6, off offset:1600 sc0 sc1
	s_and_saveexec_b64 s[24:25], s[4:5]
	s_cbranch_execz .LBB1_53
	ds_read_b32 v1, v128 offset:128
	s_mov_b64 s[20:21], exec
	s_waitcnt lgkmcnt(0)
	v_add_f32_e32 v75, v0, v1

.LBB1_54:
	ds_read2st64_b32 v[0:1], v127 offset0:80 offset1:81
	ds_read2st64_b32 v[18:19], v127 offset0:82 offset1:83
	ds_read2st64_b32 v[20:21], v127 offset0:84 offset1:85
	ds_read2st64_b32 v[22:23], v127 offset0:86 offset1:87
	v_lshlrev_b32_e32 v122, 1, v124
	v_lshl_add_u64 v[24:25], s[18:19], 0, v[122:123]
	s_waitcnt lgkmcnt(2)
	v_add_f32_e32 v18, v36, v18
	v_add_f32_e32 v0, v34, v0
	v_cvt_f16_f32_e32 v0, v0
	v_add_f32_e32 v1, v35, v1
	v_cvt_f16_f32_e32 v1, v1
	v_cvt_f16_f32_e32 v18, v18
	v_add_f32_e32 v19, v37, v19
	v_cvt_f16_f32_e32 v19, v19
	global_store_short v122, v0, s[18:19] sc0 sc1
	global_store_short v122, v1, s[18:19] offset:512 sc0 sc1
	global_store_short v122, v18, s[18:19] offset:1024 sc0 sc1
	global_store_short v122, v19, s[18:19] offset:1536 sc0 sc1
	s_waitcnt lgkmcnt(1)
	v_add_f32_e32 v0, v38, v20
	v_cvt_f16_f32_e32 v20, v0
	v_add_co_u32_e32 v0, vcc, s40, v24
	s_nop 1
	v_addc_co_u32_e32 v1, vcc, 0, v25, vcc
	v_add_co_u32_e32 v18, vcc, s35, v24
	s_nop 1
	v_addc_co_u32_e32 v19, vcc, 0, v25, vcc
	global_store_short v[18:19], v20, off offset:-4096 sc0 sc1
	v_add_f32_e32 v20, v39, v21
	v_cvt_f16_f32_e32 v20, v20
	s_waitcnt lgkmcnt(0)
	v_add_f32_e32 v21, v40, v22
	v_cvt_f16_f32_e32 v21, v21
	v_add_f32_e32 v22, v41, v23
	v_cvt_f16_f32_e32 v22, v22
	global_store_short v[0:1], v20, off offset:512 sc0 sc1
	global_store_short v[0:1], v21, off offset:1024 sc0 sc1
	ds_read2st64_b32 v[20:21], v127 offset0:88 offset1:89
	global_store_short v[0:1], v22, off offset:1536 sc0 sc1
	ds_read2st64_b32 v[22:23], v127 offset0:90 offset1:91
	ds_read2st64_b32 v[26:27], v127 offset0:92 offset1:93
	ds_read2st64_b32 v[28:29], v127 offset0:94 offset1:95
	s_waitcnt lgkmcnt(3)
	v_add_f32_e32 v20, v42, v20
	v_cvt_f16_f32_e32 v20, v20
	v_add_f32_e32 v21, v43, v21
	v_cvt_f16_f32_e32 v21, v21
	s_waitcnt lgkmcnt(2)
	v_add_f32_e32 v22, v44, v22
	v_cvt_f16_f32_e32 v22, v22
	v_add_f32_e32 v23, v45, v23
	v_cvt_f16_f32_e32 v23, v23
	global_store_short v[18:19], v20, off sc0 sc1
	global_store_short v[18:19], v21, off offset:512 sc0 sc1
	global_store_short v[18:19], v22, off offset:1024 sc0 sc1
	global_store_short v[18:19], v23, off offset:1536 sc0 sc1
	s_waitcnt lgkmcnt(1)
	v_add_f32_e32 v20, v46, v26
	v_cvt_f16_f32_e32 v22, v20
	v_add_co_u32_e32 v20, vcc, s41, v24
	s_waitcnt lgkmcnt(0)
	v_add_f32_e32 v24, v49, v29
	v_addc_co_u32_e32 v21, vcc, 0, v25, vcc
	global_store_short v[20:21], v22, off sc0 sc1
	v_add_f32_e32 v22, v47, v27
	v_cvt_f16_f32_e32 v30, v22
	v_add_f32_e32 v22, v48, v28
	v_cvt_f16_f32_e32 v31, v22
	ds_read2st64_b32 v[22:23], v127 offset0:96 offset1:97
	v_cvt_f16_f32_e32 v32, v24
	ds_read2st64_b32 v[24:25], v127 offset0:98 offset1:99
	ds_read2st64_b32 v[26:27], v127 offset0:100 offset1:101
	ds_read2st64_b32 v[28:29], v127 offset0:102 offset1:103
	s_waitcnt lgkmcnt(3)
	v_add_f32_e32 v2, v2, v22
	v_cvt_f16_f32_e32 v2, v2
	global_store_short v[20:21], v30, off offset:512 sc0 sc1
	global_store_short v[20:21], v31, off offset:1024 sc0 sc1
	global_store_short v[20:21], v32, off offset:1536 sc0 sc1
	global_store_short v122, v2, s[18:19] offset:64 sc0 sc1
	v_add_f32_e32 v2, v3, v23
	v_cvt_f16_f32_e32 v2, v2
	s_waitcnt lgkmcnt(2)
	v_add_f32_e32 v3, v4, v24
	v_cvt_f16_f32_e32 v3, v3
	v_add_f32_e32 v4, v5, v25
	v_cvt_f16_f32_e32 v4, v4
	s_waitcnt lgkmcnt(1)
	v_add_f32_e32 v5, v6, v26
	v_cvt_f16_f32_e32 v5, v5
	global_store_short v122, v2, s[18:19] offset:576 sc0 sc1
	global_store_short v122, v3, s[18:19] offset:1088 sc0 sc1
	global_store_short v122, v4, s[18:19] offset:1600 sc0 sc1
	global_store_short v[0:1], v5, off offset:64 sc0 sc1
	v_add_f32_e32 v2, v7, v27
	v_cvt_f16_f32_e32 v2, v2
	s_waitcnt lgkmcnt(0)
	v_add_f32_e32 v3, v8, v28
	v_cvt_f16_f32_e32 v3, v3
	v_add_f32_e32 v4, v9, v29
	v_cvt_f16_f32_e32 v4, v4
	global_store_short v[0:1], v2, off offset:576 sc0 sc1
	global_store_short v[0:1], v3, off offset:1088 sc0 sc1
	ds_read2st64_b32 v[2:3], v127 offset0:104 offset1:105
	s_mov_b64 s[18:19], s[20:21]
	global_store_short v[0:1], v4, off offset:1600 sc0 sc1
	ds_read2st64_b32 v[0:1], v127 offset0:106 offset1:107
	ds_read2st64_b32 v[4:5], v127 offset0:108 offset1:109
	ds_read2st64_b32 v[6:7], v127 offset0:110 offset1:111
	s_waitcnt lgkmcnt(3)
	v_add_f32_e32 v2, v10, v2
	v_cvt_f16_f32_e32 v2, v2
	v_add_f32_e32 v3, v11, v3
	v_cvt_f16_f32_e32 v3, v3
	s_waitcnt lgkmcnt(2)
	v_add_f32_e32 v0, v12, v0
	v_cvt_f16_f32_e32 v0, v0
	v_add_f32_e32 v1, v13, v1
	v_cvt_f16_f32_e32 v1, v1
	global_store_short v[18:19], v2, off offset:64 sc0 sc1
	global_store_short v[18:19], v3, off offset:576 sc0 sc1
	global_store_short v[18:19], v0, off offset:1088 sc0 sc1
	global_store_short v[18:19], v1, off offset:1600 sc0 sc1
	s_waitcnt lgkmcnt(1)
	v_add_f32_e32 v0, v14, v4
	v_cvt_f16_f32_e32 v0, v0
	v_add_f32_e32 v1, v15, v5
	v_cvt_f16_f32_e32 v1, v1
	s_waitcnt lgkmcnt(0)
	v_add_f32_e32 v2, v16, v6
	v_cvt_f16_f32_e32 v2, v2
	v_add_f32_e32 v3, v17, v7
	v_cvt_f16_f32_e32 v3, v3
	global_store_short v[20:21], v0, off offset:64 sc0 sc1
	global_store_short v[20:21], v1, off offset:576 sc0 sc1
	global_store_short v[20:21], v2, off offset:1088 sc0 sc1
	global_store_short v[20:21], v3, off offset:1600 sc0 sc1
	s_and_saveexec_b64 s[24:25], s[4:5]
	s_cbranch_execz .LBB1_56
	ds_read_b32 v0, v128
	s_or_b64 s[18:19], s[20:21], exec
	s_waitcnt lgkmcnt(0)
	v_add_f32_e32 v75, v74, v0

.LBB1_57:
	ds_read2st64_b32 v[2:3], v127 offset0:112 offset1:113
	ds_read2st64_b32 v[4:5], v127 offset0:114 offset1:115
	ds_read2st64_b32 v[6:7], v127 offset0:116 offset1:117
	ds_read2st64_b32 v[8:9], v127 offset0:118 offset1:119
	v_lshlrev_b32_e32 v1, 1, v118
	v_lshlrev_b32_e32 v122, 1, v116
	s_waitcnt lgkmcnt(3)
	v_add_f32_e32 v2, v50, v2
	v_cvt_f16_f32_e32 v2, v2
	v_add_f32_e32 v3, v51, v3
	v_cvt_f16_f32_e32 v12, v3
	global_store_short v1, v2, s[18:19] sc0 sc1
	s_waitcnt lgkmcnt(2)
	v_add_f32_e32 v1, v52, v4
	v_lshl_add_u64 v[2:3], s[18:19], 0, v[122:123]
	v_cvt_f16_f32_e32 v1, v1
	v_add_f32_e32 v4, v53, v5
	v_add_co_u32_e32 v10, vcc, 0x4000, v2
	v_cvt_f16_f32_e32 v4, v4
	s_nop 0
	v_addc_co_u32_e32 v11, vcc, 0, v3, vcc
	global_store_short v[10:11], v12, off offset:512 sc0 sc1
	global_store_short v[10:11], v1, off offset:1024 sc0 sc1
	global_store_short v[10:11], v4, off offset:1536 sc0 sc1
	s_waitcnt lgkmcnt(1)
	v_add_f32_e32 v1, v54, v6
	v_cvt_f16_f32_e32 v1, v1
	v_add_co_u32_e32 v4, vcc, s37, v2
	s_waitcnt lgkmcnt(0)
	v_add_f32_e32 v6, v56, v8
	v_addc_co_u32_e32 v5, vcc, 0, v3, vcc
	v_add_co_u32_e32 v12, vcc, s38, v2
	v_cvt_f16_f32_e32 v6, v6
	s_nop 0
	v_addc_co_u32_e32 v13, vcc, 0, v3, vcc
	global_store_short v[12:13], v1, off offset:-4096 sc0 sc1
	v_add_f32_e32 v1, v55, v7
	v_cvt_f16_f32_e32 v1, v1
	v_add_f32_e32 v7, v57, v9
	v_cvt_f16_f32_e32 v8, v7
	global_store_short v[4:5], v1, off offset:512 sc0 sc1
	global_store_short v[4:5], v6, off offset:1024 sc0 sc1
	ds_read2st64_b32 v[6:7], v127 offset0:120 offset1:121
	global_store_short v[4:5], v8, off offset:1536 sc0 sc1
	ds_read2st64_b32 v[8:9], v127 offset0:122 offset1:123
	ds_read2st64_b32 v[14:15], v127 offset0:124 offset1:125
	ds_read2st64_b32 v[16:17], v127 offset0:126 offset1:127
	v_add_co_u32_e32 v2, vcc, s39, v2
	s_waitcnt lgkmcnt(3)
	v_add_f32_e32 v1, v58, v6
	v_cvt_f16_f32_e32 v1, v1
	v_add_f32_e32 v6, v59, v7
	v_cvt_f16_f32_e32 v6, v6
	s_waitcnt lgkmcnt(2)
	v_add_f32_e32 v7, v60, v8
	v_cvt_f16_f32_e32 v7, v7
	v_add_f32_e32 v8, v61, v9
	v_cvt_f16_f32_e32 v8, v8
	global_store_short v[12:13], v1, off sc0 sc1
	global_store_short v[12:13], v6, off offset:512 sc0 sc1
	global_store_short v[12:13], v7, off offset:1024 sc0 sc1
	global_store_short v[12:13], v8, off offset:1536 sc0 sc1
	s_waitcnt lgkmcnt(1)
	v_add_f32_e32 v1, v62, v14
	v_cvt_f16_f32_e32 v1, v1
	s_waitcnt lgkmcnt(0)
	v_add_f32_e32 v6, v64, v16
	v_cvt_f16_f32_e32 v34, v6
	ds_read2st64_b32 v[6:7], v127 offset0:128 offset1:129
	v_addc_co_u32_e32 v3, vcc, 0, v3, vcc
	global_store_short v[2:3], v1, off sc0 sc1
	v_add_f32_e32 v1, v63, v15
	v_cvt_f16_f32_e32 v1, v1
	v_add_f32_e32 v8, v65, v17
	v_cvt_f16_f32_e32 v35, v8
	ds_read2st64_b32 v[8:9], v127 offset0:130 offset1:131
	ds_read2st64_b32 v[14:15], v127 offset0:132 offset1:133
	ds_read2st64_b32 v[16:17], v127 offset0:134 offset1:135
	s_waitcnt lgkmcnt(3)
	v_add_f32_e32 v6, v18, v6
	v_cvt_f16_f32_e32 v6, v6
	global_store_short v[2:3], v1, off offset:512 sc0 sc1
	global_store_short v[2:3], v34, off offset:1024 sc0 sc1
	global_store_short v[2:3], v35, off offset:1536 sc0 sc1
	global_store_short v[10:11], v6, off offset:64 sc0 sc1
	v_add_f32_e32 v1, v19, v7
	v_cvt_f16_f32_e32 v1, v1
	s_waitcnt lgkmcnt(2)
	v_add_f32_e32 v6, v20, v8
	v_cvt_f16_f32_e32 v6, v6
	v_add_f32_e32 v7, v21, v9
	v_cvt_f16_f32_e32 v7, v7
	s_waitcnt lgkmcnt(1)
	v_add_f32_e32 v8, v22, v14
	v_cvt_f16_f32_e32 v8, v8
	global_store_short v[10:11], v1, off offset:576 sc0 sc1
	global_store_short v[10:11], v6, off offset:1088 sc0 sc1
	global_store_short v[10:11], v7, off offset:1600 sc0 sc1
	global_store_short v[4:5], v8, off offset:64 sc0 sc1
	v_add_f32_e32 v1, v23, v15
	v_cvt_f16_f32_e32 v1, v1
	s_waitcnt lgkmcnt(0)
	v_add_f32_e32 v6, v24, v16
	v_cvt_f16_f32_e32 v6, v6
	v_add_f32_e32 v7, v25, v17
	v_cvt_f16_f32_e32 v8, v7
	global_store_short v[4:5], v1, off offset:576 sc0 sc1
	global_store_short v[4:5], v6, off offset:1088 sc0 sc1
	ds_read2st64_b32 v[6:7], v127 offset0:136 offset1:137
	global_store_short v[4:5], v8, off offset:1600 sc0 sc1
	ds_read2st64_b32 v[4:5], v127 offset0:138 offset1:139
	ds_read2st64_b32 v[8:9], v127 offset0:140 offset1:141
	ds_read2st64_b32 v[10:11], v127 offset0:142 offset1:143
	s_waitcnt lgkmcnt(3)
	v_add_f32_e32 v1, v26, v6
	v_cvt_f16_f32_e32 v1, v1
	v_add_f32_e32 v6, v27, v7
	v_cvt_f16_f32_e32 v6, v6
	s_waitcnt lgkmcnt(2)
	v_add_f32_e32 v4, v28, v4
	v_cvt_f16_f32_e32 v4, v4
	v_add_f32_e32 v5, v29, v5
	v_cvt_f16_f32_e32 v5, v5
	global_store_short v[12:13], v1, off offset:64 sc0 sc1
	global_store_short v[12:13], v6, off offset:576 sc0 sc1
	global_store_short v[12:13], v4, off offset:1088 sc0 sc1
	global_store_short v[12:13], v5, off offset:1600 sc0 sc1
	s_waitcnt lgkmcnt(1)
	v_add_f32_e32 v1, v30, v8
	v_cvt_f16_f32_e32 v1, v1
	v_add_f32_e32 v4, v31, v9
	v_cvt_f16_f32_e32 v4, v4
	s_waitcnt lgkmcnt(0)
	v_add_f32_e32 v5, v32, v10
	v_cvt_f16_f32_e32 v5, v5
	v_add_f32_e32 v6, v33, v11
	v_cvt_f16_f32_e32 v6, v6
	global_store_short v[2:3], v1, off offset:64 sc0 sc1
	global_store_short v[2:3], v4, off offset:576 sc0 sc1
	global_store_short v[2:3], v5, off offset:1088 sc0 sc1
	global_store_short v[2:3], v6, off offset:1600 sc0 sc1
	s_and_saveexec_b64 s[24:25], s[4:5]
	s_cbranch_execz .LBB1_59
	ds_read_b32 v1, v128 offset:128
	s_mov_b64 s[20:21], exec
	s_waitcnt lgkmcnt(0)
	v_add_f32_e32 v99, v0, v1

.LBB1_60:
	ds_read2st64_b32 v[0:1], v127 offset0:80 offset1:81
	ds_read2st64_b32 v[18:19], v127 offset0:82 offset1:83
	ds_read2st64_b32 v[20:21], v127 offset0:84 offset1:85
	ds_read2st64_b32 v[22:23], v127 offset0:86 offset1:87
	v_lshlrev_b32_e32 v122, 1, v124
	v_lshl_add_u64 v[24:25], s[18:19], 0, v[122:123]
	s_waitcnt lgkmcnt(2)
	v_add_f32_e32 v18, v36, v18
	v_add_f32_e32 v0, v34, v0
	v_cvt_f16_f32_e32 v0, v0
	v_add_f32_e32 v1, v35, v1
	v_cvt_f16_f32_e32 v1, v1
	v_cvt_f16_f32_e32 v18, v18
	v_add_f32_e32 v19, v37, v19
	v_cvt_f16_f32_e32 v19, v19
	global_store_short v122, v0, s[18:19] sc0 sc1
	global_store_short v122, v1, s[18:19] offset:512 sc0 sc1
	global_store_short v122, v18, s[18:19] offset:1024 sc0 sc1
	global_store_short v122, v19, s[18:19] offset:1536 sc0 sc1
	s_waitcnt lgkmcnt(1)
	v_add_f32_e32 v0, v38, v20
	v_cvt_f16_f32_e32 v20, v0
	v_add_co_u32_e32 v0, vcc, s40, v24
	s_nop 1
	v_addc_co_u32_e32 v1, vcc, 0, v25, vcc
	v_add_co_u32_e32 v18, vcc, s35, v24
	s_nop 1
	v_addc_co_u32_e32 v19, vcc, 0, v25, vcc
	global_store_short v[18:19], v20, off offset:-4096 sc0 sc1
	v_add_f32_e32 v20, v39, v21
	v_cvt_f16_f32_e32 v20, v20
	s_waitcnt lgkmcnt(0)
	v_add_f32_e32 v21, v40, v22
	v_cvt_f16_f32_e32 v21, v21
	v_add_f32_e32 v22, v41, v23
	v_cvt_f16_f32_e32 v22, v22
	global_store_short v[0:1], v20, off offset:512 sc0 sc1
	global_store_short v[0:1], v21, off offset:1024 sc0 sc1
	ds_read2st64_b32 v[20:21], v127 offset0:88 offset1:89
	global_store_short v[0:1], v22, off offset:1536 sc0 sc1
	ds_read2st64_b32 v[22:23], v127 offset0:90 offset1:91
	ds_read2st64_b32 v[26:27], v127 offset0:92 offset1:93
	ds_read2st64_b32 v[28:29], v127 offset0:94 offset1:95
	s_waitcnt lgkmcnt(3)
	v_add_f32_e32 v20, v42, v20
	v_cvt_f16_f32_e32 v20, v20
	v_add_f32_e32 v21, v43, v21
	v_cvt_f16_f32_e32 v21, v21
	s_waitcnt lgkmcnt(2)
	v_add_f32_e32 v22, v44, v22
	v_cvt_f16_f32_e32 v22, v22
	v_add_f32_e32 v23, v45, v23
	v_cvt_f16_f32_e32 v23, v23
	global_store_short v[18:19], v20, off sc0 sc1
	global_store_short v[18:19], v21, off offset:512 sc0 sc1
	global_store_short v[18:19], v22, off offset:1024 sc0 sc1
	global_store_short v[18:19], v23, off offset:1536 sc0 sc1
	s_waitcnt lgkmcnt(1)
	v_add_f32_e32 v20, v46, v26
	v_cvt_f16_f32_e32 v22, v20
	v_add_co_u32_e32 v20, vcc, s41, v24
	s_waitcnt lgkmcnt(0)
	v_add_f32_e32 v24, v49, v29
	v_addc_co_u32_e32 v21, vcc, 0, v25, vcc
	global_store_short v[20:21], v22, off sc0 sc1
	v_add_f32_e32 v22, v47, v27
	v_cvt_f16_f32_e32 v30, v22
	v_add_f32_e32 v22, v48, v28
	v_cvt_f16_f32_e32 v31, v22
	ds_read2st64_b32 v[22:23], v127 offset0:96 offset1:97
	v_cvt_f16_f32_e32 v32, v24
	ds_read2st64_b32 v[24:25], v127 offset0:98 offset1:99
	ds_read2st64_b32 v[26:27], v127 offset0:100 offset1:101
	ds_read2st64_b32 v[28:29], v127 offset0:102 offset1:103
	s_waitcnt lgkmcnt(3)
	v_add_f32_e32 v2, v2, v22
	v_cvt_f16_f32_e32 v2, v2
	global_store_short v[20:21], v30, off offset:512 sc0 sc1
	global_store_short v[20:21], v31, off offset:1024 sc0 sc1
	global_store_short v[20:21], v32, off offset:1536 sc0 sc1
	global_store_short v122, v2, s[18:19] offset:64 sc0 sc1
	v_add_f32_e32 v2, v3, v23
	v_cvt_f16_f32_e32 v2, v2
	s_waitcnt lgkmcnt(2)
	v_add_f32_e32 v3, v4, v24
	v_cvt_f16_f32_e32 v3, v3
	v_add_f32_e32 v4, v5, v25
	v_cvt_f16_f32_e32 v4, v4
	s_waitcnt lgkmcnt(1)
	v_add_f32_e32 v5, v6, v26
	v_cvt_f16_f32_e32 v5, v5
	global_store_short v122, v2, s[18:19] offset:576 sc0 sc1
	global_store_short v122, v3, s[18:19] offset:1088 sc0 sc1
	global_store_short v122, v4, s[18:19] offset:1600 sc0 sc1
	global_store_short v[0:1], v5, off offset:64 sc0 sc1
	v_add_f32_e32 v2, v7, v27
	v_cvt_f16_f32_e32 v2, v2
	s_waitcnt lgkmcnt(0)
	v_add_f32_e32 v3, v8, v28
	v_cvt_f16_f32_e32 v3, v3
	v_add_f32_e32 v4, v9, v29
	v_cvt_f16_f32_e32 v4, v4
	global_store_short v[0:1], v2, off offset:576 sc0 sc1
	global_store_short v[0:1], v3, off offset:1088 sc0 sc1
	ds_read2st64_b32 v[2:3], v127 offset0:104 offset1:105
	s_mov_b64 s[18:19], s[20:21]
	global_store_short v[0:1], v4, off offset:1600 sc0 sc1
	ds_read2st64_b32 v[0:1], v127 offset0:106 offset1:107
	ds_read2st64_b32 v[4:5], v127 offset0:108 offset1:109
	ds_read2st64_b32 v[6:7], v127 offset0:110 offset1:111
	s_waitcnt lgkmcnt(3)
	v_add_f32_e32 v2, v10, v2
	v_cvt_f16_f32_e32 v2, v2
	v_add_f32_e32 v3, v11, v3
	v_cvt_f16_f32_e32 v3, v3
	s_waitcnt lgkmcnt(2)
	v_add_f32_e32 v0, v12, v0
	v_cvt_f16_f32_e32 v0, v0
	v_add_f32_e32 v1, v13, v1
	v_cvt_f16_f32_e32 v1, v1
	global_store_short v[18:19], v2, off offset:64 sc0 sc1
	global_store_short v[18:19], v3, off offset:576 sc0 sc1
	global_store_short v[18:19], v0, off offset:1088 sc0 sc1
	global_store_short v[18:19], v1, off offset:1600 sc0 sc1
	s_waitcnt lgkmcnt(1)
	v_add_f32_e32 v0, v14, v4
	v_cvt_f16_f32_e32 v0, v0
	v_add_f32_e32 v1, v15, v5
	v_cvt_f16_f32_e32 v1, v1
	s_waitcnt lgkmcnt(0)
	v_add_f32_e32 v2, v16, v6
	v_cvt_f16_f32_e32 v2, v2
	v_add_f32_e32 v3, v17, v7
	v_cvt_f16_f32_e32 v3, v3
	global_store_short v[20:21], v0, off offset:64 sc0 sc1
	global_store_short v[20:21], v1, off offset:576 sc0 sc1
	global_store_short v[20:21], v2, off offset:1088 sc0 sc1
	global_store_short v[20:21], v3, off offset:1600 sc0 sc1
	s_and_saveexec_b64 s[24:25], s[4:5]
	s_cbranch_execz .LBB1_62
	ds_read_b32 v0, v128
	s_or_b64 s[18:19], s[20:21], exec
	s_waitcnt lgkmcnt(0)
	v_add_f32_e32 v99, v98, v0

.LBB1_63:
	s_lshl_b64 s[16:17], s[16:17], 10
	s_add_u32 s16, s14, s16
	s_addc_u32 s17, s15, s17
	v_lshlrev_b32_e32 v0, 2, v0
	global_store_dword v0, v99, s[16:17] sc0 sc1
	s_or_b64 exec, exec, s[18:19]
	s_cmp_gt_u32 s42, 23
	s_cbranch_scc1 .LBB1_2
